# HGRN2 H1 chunk loop: 14 v_pk_mul_f32 between MFMAs split into scalar v_mul_f32 pairs (bit-identical)
# speedup vs baseline: 1.0048x; 1.0048x over previous
.LBB0_577:
	v_add_u32_e32 v46, s49, v72
	ds_read_b128 v[46:49], v46
	ds_read_b128 v[50:53], v99
	v_add_f32_e32 v105, v105, v138
	s_nop 2
	v_cvt_pk_bf16_f32 v138, v42, v43
	v_cvt_pk_bf16_f32 v139, v44, v45
	s_waitcnt lgkmcnt(1)
	v_mul_f32_e32 v46, 0x3fb8aa3b, v46
	v_mul_f32_e32 v47, 0x3fb8aa3b, v47
	v_mul_f32_e32 v48, 0x3fb8aa3b, v48
	v_exp_f32_e32 v148, v46
	v_mul_f32_e32 v46, 0x3fb8aa3b, v49
	v_exp_f32_e32 v149, v47
	v_exp_f32_e32 v150, v48
	v_exp_f32_e32 v151, v46
	ds_read_b128 v[46:49], v100
	ds_read_b128 v[140:143], v99 offset:64
	v_mul_f32_e32 v14, v14, v148
	v_mul_f32_e32 v15, v15, v149
	v_mul_f32_e32 v10, v10, v148
	v_mul_f32_e32 v11, v11, v149
	v_mul_f32_e32 v16, v16, v150
	v_mul_f32_e32 v17, v17, v151
	v_mul_f32_e32 v12, v12, v150
	v_mul_f32_e32 v13, v13, v151
	v_mul_f32_e32 v8, v8, v150
	v_mul_f32_e32 v9, v9, v151
	s_waitcnt lgkmcnt(1)
	v_mfma_f32_16x16x32_bf16 v[14:17], v[50:53], v[46:49], v[14:17]
	ds_read_b128 v[46:49], v100 offset:64
	ds_read_b128 v[144:147], v100 offset:2304
	v_mul_f32_e32 v6, v6, v148
	v_mul_f32_e32 v7, v7, v149
	v_mul_f32_e32 v32, v32, v150
	v_mul_f32_e32 v33, v33, v151
	s_waitcnt lgkmcnt(1)
	v_mfma_f32_16x16x32_bf16 v[14:17], v[140:143], v[46:49], v[14:17]
	v_mul_f32_e64 v30, v30, v148
	v_mul_f32_e64 v31, v31, v149
	v_mul_f32_e32 v28, v28, v150
	v_mul_f32_e32 v29, v29, v151
	v_mul_f32_e32 v26, v26, v148
	v_mul_f32_e32 v27, v27, v149
	s_waitcnt lgkmcnt(0)
	v_mfma_f32_16x16x32_bf16 v[10:13], v[50:53], v[144:147], v[10:13]
	ds_read_b128 v[46:49], v100 offset:2368
	ds_read_b128 v[144:147], v100 offset:4608
	v_mul_f32_e32 v24, v24, v150
	v_mul_f32_e32 v25, v25, v151
	v_mul_f32_e32 v22, v22, v148
	v_mul_f32_e32 v23, v23, v149
	s_waitcnt lgkmcnt(1)
	v_mfma_f32_16x16x32_bf16 v[10:13], v[140:143], v[46:49], v[10:13]
	v_mul_f32_e64 v4, v4, v150
	v_mul_f32_e64 v5, v5, v151
	v_mul_f32_e32 v2, v2, v148
	v_mul_f32_e32 v3, v3, v149
	v_mul_f32_e32 v20, v20, v150
	v_mul_f32_e32 v21, v21, v151
	s_waitcnt lgkmcnt(0)
	v_mfma_f32_16x16x32_bf16 v[6:9], v[50:53], v[144:147], v[6:9]
	ds_read_b128 v[46:49], v100 offset:4672
	ds_read_b128 v[144:147], v100 offset:6912
	v_mul_f32_e32 v18, v18, v148
	v_mul_f32_e32 v19, v19, v149
	s_add_u32 s0, s0, 0x10000
	s_waitcnt lgkmcnt(1)
	v_mfma_f32_16x16x32_bf16 v[6:9], v[140:143], v[46:49], v[6:9]
	s_addc_u32 s1, s1, 0
	s_cmp_eq_u32 s0, 0x100000
	s_waitcnt lgkmcnt(0)
	v_mfma_f32_16x16x32_bf16 v[30:33], v[50:53], v[144:147], v[30:33]
	ds_read_b128 v[46:49], v100 offset:6976
	ds_read_b128 v[144:147], v100 offset:9216
	s_waitcnt lgkmcnt(1)
	v_mfma_f32_16x16x32_bf16 v[30:33], v[140:143], v[46:49], v[30:33]
	s_waitcnt lgkmcnt(0)
	v_mfma_f32_16x16x32_bf16 v[26:29], v[50:53], v[144:147], v[26:29]
	ds_read_b128 v[46:49], v100 offset:9280
	ds_read_b128 v[144:147], v100 offset:11520
	ds_read_b128 v[42:45], v100 offset:16128
	s_waitcnt lgkmcnt(2)
	v_mfma_f32_16x16x32_bf16 v[26:29], v[140:143], v[46:49], v[26:29]
	ds_read_b128 v[46:49], v100 offset:11584
	s_waitcnt lgkmcnt(2)
	v_mfma_f32_16x16x32_bf16 v[22:25], v[50:53], v[144:147], v[22:25]
	ds_read_b128 v[144:147], v100 offset:13824
	s_waitcnt lgkmcnt(1)
	v_mfma_f32_16x16x32_bf16 v[22:25], v[140:143], v[46:49], v[22:25]
	ds_read_b128 v[46:49], v100 offset:13888
	v_mfma_f32_16x16x32_bf16 v[2:5], v[50:53], v[42:45], v[2:5]
	ds_read_b128 v[42:45], v100 offset:16192
	s_waitcnt lgkmcnt(2)
	v_mfma_f32_16x16x32_bf16 v[18:21], v[50:53], v[144:147], v[18:21]
	s_waitcnt lgkmcnt(1)
	v_mfma_f32_16x16x32_bf16 v[18:21], v[140:143], v[46:49], v[18:21]
	v_add_co_u32_e32 v46, vcc, 0x3100c000, v68
	s_waitcnt lgkmcnt(0)
	v_mfma_f32_16x16x32_bf16 v[2:5], v[140:143], v[42:45], v[2:5]
	v_addc_co_u32_e32 v47, vcc, 0, v69, vcc
	global_store_dwordx2 v[46:47], v[138:139], off
	s_barrier
	s_cbranch_scc1 .LBB0_692
